# p3_mlstate wave-0 DN tail: 8-iteration LDS-read/fmac loop unrolled with next iteration reads issued one step ahead (second register set), same fmac order
# baseline (speedup 1.0000x reference)
.LBB0_745:
	v_mov_b32_e32 v139, s10
	ds_read_b128 v[4:7], v57 offset:0
	ds_read_b128 v[8:11], v57 offset:16
	ds_read_b128 v[12:15], v139 offset:0
	ds_read_b128 v[16:19], v139 offset:16
	ds_read_b128 v[20:23], v139 offset:32
	ds_read_b128 v[24:27], v139 offset:48
	ds_read_b128 v[198:201], v57 offset:32
	ds_read_b128 v[202:205], v57 offset:48
	ds_read_b128 v[206:209], v139 offset:64
	ds_read_b128 v[210:213], v139 offset:80
	ds_read_b128 v[214:217], v139 offset:96
	ds_read_b128 v[218:221], v139 offset:112
	s_waitcnt lgkmcnt(11)
	v_lshlrev_b32_e32 v3, 16, v4
	s_waitcnt lgkmcnt(9)
	v_fmac_f32_e32 v2, v12, v3
	v_and_b32_e32 v3, 0xffff0000, v4
	v_fmac_f32_e32 v2, v13, v3
	v_lshlrev_b32_e32 v3, 16, v5
	v_fmac_f32_e32 v2, v14, v3
	v_and_b32_e32 v3, 0xffff0000, v5
	v_fmac_f32_e32 v2, v15, v3
	v_lshlrev_b32_e32 v3, 16, v6
	s_waitcnt lgkmcnt(8)
	v_fmac_f32_e32 v2, v16, v3
	v_and_b32_e32 v3, 0xffff0000, v6
	v_fmac_f32_e32 v2, v17, v3
	v_lshlrev_b32_e32 v3, 16, v7
	v_fmac_f32_e32 v2, v18, v3
	v_and_b32_e32 v3, 0xffff0000, v7
	v_fmac_f32_e32 v2, v19, v3
	v_lshlrev_b32_e32 v3, 16, v8
	s_waitcnt lgkmcnt(7)
	v_fmac_f32_e32 v2, v20, v3
	v_and_b32_e32 v3, 0xffff0000, v8
	v_fmac_f32_e32 v2, v21, v3
	v_lshlrev_b32_e32 v3, 16, v9
	v_fmac_f32_e32 v2, v22, v3
	v_and_b32_e32 v3, 0xffff0000, v9
	v_fmac_f32_e32 v2, v23, v3
	v_lshlrev_b32_e32 v3, 16, v10
	s_waitcnt lgkmcnt(6)
	v_fmac_f32_e32 v2, v24, v3
	v_and_b32_e32 v3, 0xffff0000, v10
	v_fmac_f32_e32 v2, v25, v3
	v_lshlrev_b32_e32 v3, 16, v11
	v_fmac_f32_e32 v2, v26, v3
	v_and_b32_e32 v3, 0xffff0000, v11
	v_fmac_f32_e32 v2, v27, v3
	ds_read_b128 v[4:7], v57 offset:64
	ds_read_b128 v[8:11], v57 offset:80
	ds_read_b128 v[12:15], v139 offset:128
	ds_read_b128 v[16:19], v139 offset:144
	ds_read_b128 v[20:23], v139 offset:160
	ds_read_b128 v[24:27], v139 offset:176
	s_waitcnt lgkmcnt(11)
	v_lshlrev_b32_e32 v3, 16, v198
	s_waitcnt lgkmcnt(9)
	v_fmac_f32_e32 v2, v206, v3
	v_and_b32_e32 v3, 0xffff0000, v198
	v_fmac_f32_e32 v2, v207, v3
	v_lshlrev_b32_e32 v3, 16, v199
	v_fmac_f32_e32 v2, v208, v3
	v_and_b32_e32 v3, 0xffff0000, v199
	v_fmac_f32_e32 v2, v209, v3
	v_lshlrev_b32_e32 v3, 16, v200
	s_waitcnt lgkmcnt(8)
	v_fmac_f32_e32 v2, v210, v3
	v_and_b32_e32 v3, 0xffff0000, v200
	v_fmac_f32_e32 v2, v211, v3
	v_lshlrev_b32_e32 v3, 16, v201
	v_fmac_f32_e32 v2, v212, v3
	v_and_b32_e32 v3, 0xffff0000, v201
	v_fmac_f32_e32 v2, v213, v3
	v_lshlrev_b32_e32 v3, 16, v202
	s_waitcnt lgkmcnt(7)
	v_fmac_f32_e32 v2, v214, v3
	v_and_b32_e32 v3, 0xffff0000, v202
	v_fmac_f32_e32 v2, v215, v3
	v_lshlrev_b32_e32 v3, 16, v203
	v_fmac_f32_e32 v2, v216, v3
	v_and_b32_e32 v3, 0xffff0000, v203
	v_fmac_f32_e32 v2, v217, v3
	v_lshlrev_b32_e32 v3, 16, v204
	s_waitcnt lgkmcnt(6)
	v_fmac_f32_e32 v2, v218, v3
	v_and_b32_e32 v3, 0xffff0000, v204
	v_fmac_f32_e32 v2, v219, v3
	v_lshlrev_b32_e32 v3, 16, v205
	v_fmac_f32_e32 v2, v220, v3
	v_and_b32_e32 v3, 0xffff0000, v205
	v_fmac_f32_e32 v2, v221, v3
	ds_read_b128 v[198:201], v57 offset:96
	ds_read_b128 v[202:205], v57 offset:112
	ds_read_b128 v[206:209], v139 offset:192
	ds_read_b128 v[210:213], v139 offset:208
	ds_read_b128 v[214:217], v139 offset:224
	ds_read_b128 v[218:221], v139 offset:240
	s_waitcnt lgkmcnt(11)
	v_lshlrev_b32_e32 v3, 16, v4
	s_waitcnt lgkmcnt(9)
	v_fmac_f32_e32 v2, v12, v3
	v_and_b32_e32 v3, 0xffff0000, v4
	v_fmac_f32_e32 v2, v13, v3
	v_lshlrev_b32_e32 v3, 16, v5
	v_fmac_f32_e32 v2, v14, v3
	v_and_b32_e32 v3, 0xffff0000, v5
	v_fmac_f32_e32 v2, v15, v3
	v_lshlrev_b32_e32 v3, 16, v6
	s_waitcnt lgkmcnt(8)
	v_fmac_f32_e32 v2, v16, v3
	v_and_b32_e32 v3, 0xffff0000, v6
	v_fmac_f32_e32 v2, v17, v3
	v_lshlrev_b32_e32 v3, 16, v7
	v_fmac_f32_e32 v2, v18, v3
	v_and_b32_e32 v3, 0xffff0000, v7
	v_fmac_f32_e32 v2, v19, v3
	v_lshlrev_b32_e32 v3, 16, v8
	s_waitcnt lgkmcnt(7)
	v_fmac_f32_e32 v2, v20, v3
	v_and_b32_e32 v3, 0xffff0000, v8
	v_fmac_f32_e32 v2, v21, v3
	v_lshlrev_b32_e32 v3, 16, v9
	v_fmac_f32_e32 v2, v22, v3
	v_and_b32_e32 v3, 0xffff0000, v9
	v_fmac_f32_e32 v2, v23, v3
	v_lshlrev_b32_e32 v3, 16, v10
	s_waitcnt lgkmcnt(6)
	v_fmac_f32_e32 v2, v24, v3
	v_and_b32_e32 v3, 0xffff0000, v10
	v_fmac_f32_e32 v2, v25, v3
	v_lshlrev_b32_e32 v3, 16, v11
	v_fmac_f32_e32 v2, v26, v3
	v_and_b32_e32 v3, 0xffff0000, v11
	v_fmac_f32_e32 v2, v27, v3
	ds_read_b128 v[4:7], v57 offset:128
	ds_read_b128 v[8:11], v57 offset:144
	ds_read_b128 v[12:15], v139 offset:256
	ds_read_b128 v[16:19], v139 offset:272
	ds_read_b128 v[20:23], v139 offset:288
	ds_read_b128 v[24:27], v139 offset:304
	s_waitcnt lgkmcnt(11)
	v_lshlrev_b32_e32 v3, 16, v198
	s_waitcnt lgkmcnt(9)
	v_fmac_f32_e32 v2, v206, v3
	v_and_b32_e32 v3, 0xffff0000, v198
	v_fmac_f32_e32 v2, v207, v3
	v_lshlrev_b32_e32 v3, 16, v199
	v_fmac_f32_e32 v2, v208, v3
	v_and_b32_e32 v3, 0xffff0000, v199
	v_fmac_f32_e32 v2, v209, v3
	v_lshlrev_b32_e32 v3, 16, v200
	s_waitcnt lgkmcnt(8)
	v_fmac_f32_e32 v2, v210, v3
	v_and_b32_e32 v3, 0xffff0000, v200
	v_fmac_f32_e32 v2, v211, v3
	v_lshlrev_b32_e32 v3, 16, v201
	v_fmac_f32_e32 v2, v212, v3
	v_and_b32_e32 v3, 0xffff0000, v201
	v_fmac_f32_e32 v2, v213, v3
	v_lshlrev_b32_e32 v3, 16, v202
	s_waitcnt lgkmcnt(7)
	v_fmac_f32_e32 v2, v214, v3
	v_and_b32_e32 v3, 0xffff0000, v202
	v_fmac_f32_e32 v2, v215, v3
	v_lshlrev_b32_e32 v3, 16, v203
	v_fmac_f32_e32 v2, v216, v3
	v_and_b32_e32 v3, 0xffff0000, v203
	v_fmac_f32_e32 v2, v217, v3
	v_lshlrev_b32_e32 v3, 16, v204
	s_waitcnt lgkmcnt(6)
	v_fmac_f32_e32 v2, v218, v3
	v_and_b32_e32 v3, 0xffff0000, v204
	v_fmac_f32_e32 v2, v219, v3
	v_lshlrev_b32_e32 v3, 16, v205
	v_fmac_f32_e32 v2, v220, v3
	v_and_b32_e32 v3, 0xffff0000, v205
	v_fmac_f32_e32 v2, v221, v3
	ds_read_b128 v[198:201], v57 offset:160
	ds_read_b128 v[202:205], v57 offset:176
	ds_read_b128 v[206:209], v139 offset:320
	ds_read_b128 v[210:213], v139 offset:336
	ds_read_b128 v[214:217], v139 offset:352
	ds_read_b128 v[218:221], v139 offset:368
	s_waitcnt lgkmcnt(11)
	v_lshlrev_b32_e32 v3, 16, v4
	s_waitcnt lgkmcnt(9)
	v_fmac_f32_e32 v2, v12, v3
	v_and_b32_e32 v3, 0xffff0000, v4
	v_fmac_f32_e32 v2, v13, v3
	v_lshlrev_b32_e32 v3, 16, v5
	v_fmac_f32_e32 v2, v14, v3
	v_and_b32_e32 v3, 0xffff0000, v5
	v_fmac_f32_e32 v2, v15, v3
	v_lshlrev_b32_e32 v3, 16, v6
	s_waitcnt lgkmcnt(8)
	v_fmac_f32_e32 v2, v16, v3
	v_and_b32_e32 v3, 0xffff0000, v6
	v_fmac_f32_e32 v2, v17, v3
	v_lshlrev_b32_e32 v3, 16, v7
	v_fmac_f32_e32 v2, v18, v3
	v_and_b32_e32 v3, 0xffff0000, v7
	v_fmac_f32_e32 v2, v19, v3
	v_lshlrev_b32_e32 v3, 16, v8
	s_waitcnt lgkmcnt(7)
	v_fmac_f32_e32 v2, v20, v3
	v_and_b32_e32 v3, 0xffff0000, v8
	v_fmac_f32_e32 v2, v21, v3
	v_lshlrev_b32_e32 v3, 16, v9
	v_fmac_f32_e32 v2, v22, v3
	v_and_b32_e32 v3, 0xffff0000, v9
	v_fmac_f32_e32 v2, v23, v3
	v_lshlrev_b32_e32 v3, 16, v10
	s_waitcnt lgkmcnt(6)
	v_fmac_f32_e32 v2, v24, v3
	v_and_b32_e32 v3, 0xffff0000, v10
	v_fmac_f32_e32 v2, v25, v3
	v_lshlrev_b32_e32 v3, 16, v11
	v_fmac_f32_e32 v2, v26, v3
	v_and_b32_e32 v3, 0xffff0000, v11
	v_fmac_f32_e32 v2, v27, v3
	ds_read_b128 v[4:7], v57 offset:192
	ds_read_b128 v[8:11], v57 offset:208
	ds_read_b128 v[12:15], v139 offset:384
	ds_read_b128 v[16:19], v139 offset:400
	ds_read_b128 v[20:23], v139 offset:416
	ds_read_b128 v[24:27], v139 offset:432
	s_waitcnt lgkmcnt(11)
	v_lshlrev_b32_e32 v3, 16, v198
	s_waitcnt lgkmcnt(9)
	v_fmac_f32_e32 v2, v206, v3
	v_and_b32_e32 v3, 0xffff0000, v198
	v_fmac_f32_e32 v2, v207, v3
	v_lshlrev_b32_e32 v3, 16, v199
	v_fmac_f32_e32 v2, v208, v3
	v_and_b32_e32 v3, 0xffff0000, v199
	v_fmac_f32_e32 v2, v209, v3
	v_lshlrev_b32_e32 v3, 16, v200
	s_waitcnt lgkmcnt(8)
	v_fmac_f32_e32 v2, v210, v3
	v_and_b32_e32 v3, 0xffff0000, v200
	v_fmac_f32_e32 v2, v211, v3
	v_lshlrev_b32_e32 v3, 16, v201
	v_fmac_f32_e32 v2, v212, v3
	v_and_b32_e32 v3, 0xffff0000, v201
	v_fmac_f32_e32 v2, v213, v3
	v_lshlrev_b32_e32 v3, 16, v202
	s_waitcnt lgkmcnt(7)
	v_fmac_f32_e32 v2, v214, v3
	v_and_b32_e32 v3, 0xffff0000, v202
	v_fmac_f32_e32 v2, v215, v3
	v_lshlrev_b32_e32 v3, 16, v203
	v_fmac_f32_e32 v2, v216, v3
	v_and_b32_e32 v3, 0xffff0000, v203
	v_fmac_f32_e32 v2, v217, v3
	v_lshlrev_b32_e32 v3, 16, v204
	s_waitcnt lgkmcnt(6)
	v_fmac_f32_e32 v2, v218, v3
	v_and_b32_e32 v3, 0xffff0000, v204
	v_fmac_f32_e32 v2, v219, v3
	v_lshlrev_b32_e32 v3, 16, v205
	v_fmac_f32_e32 v2, v220, v3
	v_and_b32_e32 v3, 0xffff0000, v205
	v_fmac_f32_e32 v2, v221, v3
	ds_read_b128 v[198:201], v57 offset:224
	ds_read_b128 v[202:205], v57 offset:240
	ds_read_b128 v[206:209], v139 offset:448
	ds_read_b128 v[210:213], v139 offset:464
	ds_read_b128 v[214:217], v139 offset:480
	ds_read_b128 v[218:221], v139 offset:496
	s_waitcnt lgkmcnt(11)
	v_lshlrev_b32_e32 v3, 16, v4
	s_waitcnt lgkmcnt(9)
	v_fmac_f32_e32 v2, v12, v3
	v_and_b32_e32 v3, 0xffff0000, v4
	v_fmac_f32_e32 v2, v13, v3
	v_lshlrev_b32_e32 v3, 16, v5
	v_fmac_f32_e32 v2, v14, v3
	v_and_b32_e32 v3, 0xffff0000, v5
	v_fmac_f32_e32 v2, v15, v3
	v_lshlrev_b32_e32 v3, 16, v6
	s_waitcnt lgkmcnt(8)
	v_fmac_f32_e32 v2, v16, v3
	v_and_b32_e32 v3, 0xffff0000, v6
	v_fmac_f32_e32 v2, v17, v3
	v_lshlrev_b32_e32 v3, 16, v7
	v_fmac_f32_e32 v2, v18, v3
	v_and_b32_e32 v3, 0xffff0000, v7
	v_fmac_f32_e32 v2, v19, v3
	v_lshlrev_b32_e32 v3, 16, v8
	s_waitcnt lgkmcnt(7)
	v_fmac_f32_e32 v2, v20, v3
	v_and_b32_e32 v3, 0xffff0000, v8
	v_fmac_f32_e32 v2, v21, v3
	v_lshlrev_b32_e32 v3, 16, v9
	v_fmac_f32_e32 v2, v22, v3
	v_and_b32_e32 v3, 0xffff0000, v9
	v_fmac_f32_e32 v2, v23, v3
	v_lshlrev_b32_e32 v3, 16, v10
	s_waitcnt lgkmcnt(6)
	v_fmac_f32_e32 v2, v24, v3
	v_and_b32_e32 v3, 0xffff0000, v10
	v_fmac_f32_e32 v2, v25, v3
	v_lshlrev_b32_e32 v3, 16, v11
	v_fmac_f32_e32 v2, v26, v3
	v_and_b32_e32 v3, 0xffff0000, v11
	v_fmac_f32_e32 v2, v27, v3
	s_waitcnt lgkmcnt(5)
	v_lshlrev_b32_e32 v3, 16, v198
	s_waitcnt lgkmcnt(3)
	v_fmac_f32_e32 v2, v206, v3
	v_and_b32_e32 v3, 0xffff0000, v198
	v_fmac_f32_e32 v2, v207, v3
	v_lshlrev_b32_e32 v3, 16, v199
	v_fmac_f32_e32 v2, v208, v3
	v_and_b32_e32 v3, 0xffff0000, v199
	v_fmac_f32_e32 v2, v209, v3
	v_lshlrev_b32_e32 v3, 16, v200
	s_waitcnt lgkmcnt(2)
	v_fmac_f32_e32 v2, v210, v3
	v_and_b32_e32 v3, 0xffff0000, v200
	v_fmac_f32_e32 v2, v211, v3
	v_lshlrev_b32_e32 v3, 16, v201
	v_fmac_f32_e32 v2, v212, v3
	v_and_b32_e32 v3, 0xffff0000, v201
	v_fmac_f32_e32 v2, v213, v3
	v_lshlrev_b32_e32 v3, 16, v202
	s_waitcnt lgkmcnt(1)
	v_fmac_f32_e32 v2, v214, v3
	v_and_b32_e32 v3, 0xffff0000, v202
	v_fmac_f32_e32 v2, v215, v3
	v_lshlrev_b32_e32 v3, 16, v203
	v_fmac_f32_e32 v2, v216, v3
	v_and_b32_e32 v3, 0xffff0000, v203
	v_fmac_f32_e32 v2, v217, v3
	v_lshlrev_b32_e32 v3, 16, v204
	s_waitcnt lgkmcnt(0)
	v_fmac_f32_e32 v2, v218, v3
	v_and_b32_e32 v3, 0xffff0000, v204
	v_fmac_f32_e32 v2, v219, v3
	v_lshlrev_b32_e32 v3, 16, v205
	v_fmac_f32_e32 v2, v220, v3
	v_and_b32_e32 v3, 0xffff0000, v205
	v_fmac_f32_e32 v2, v221, v3
	s_lshl_b64 s[0:1], s[0:1], 8
	v_lshl_add_u64 v[4:5], v[44:45], 0, s[0:1]
	global_store_dword v[4:5], v2, off
	s_or_b64 exec, exec, s[8:9]
	s_and_saveexec_b64 s[0:1], s[40:41]
	s_cbranch_execz .LBB0_727
